# speedup vs baseline: 1.0553x; 1.0009x over previous
_Z11attn_kernelPKfS0_S0_PKcS2_PKDv4_jS0_S0_S0_S0_Pf:
	s_load_dwordx8 s[4:11], s[0:1], 0x0
	s_load_dwordx8 s[12:19], s[0:1], 0x20
	v_readfirstlane_b32 s20, v0
	s_bfe_u32 s28, s2, 0x10002
	s_lshr_b32 s29, s20, 6
	s_lshr_b32 s3, s20, 8
	s_bfe_u32 s30, s20, 0x20006
	s_lshr_b32 s31, s2, 3
	s_lshl_b32 s24, s28, 18
	s_waitcnt lgkmcnt(0)
	s_add_u32 s20, s10, s24
	s_addc_u32 s10, s11, 0
	s_and_b32 s21, s10, 0xffff
	s_add_u32 s24, s12, s24
	s_addc_u32 s10, s13, 0
	v_and_b32_e32 v1, 63, v0
	s_and_b32 s25, s10, 0xffff
	s_lshl_b32 s10, s30, 10
	s_lshl_b32 s38, s3, 12
	v_lshlrev_b32_e32 v2, 4, v1
	s_or_b32 s35, s10, s38
	v_lshl_or_b32 v2, s3, 17, v2
	s_cmp_lg_u32 0, -1
	v_or_b32_e32 v174, s10, v2
	s_cselect_b32 s10, 0, 0
	s_mov_b32 s36, 0
	s_mov_b32 s23, 0x20000
	s_mov_b32 s22, 0x40000
	s_add_i32 s33, s35, s10
	s_mov_b32 m0, s33
	s_nop 0
	buffer_load_dwordx4 v174, s[20:23], s36 offen lds
	s_mov_b32 s26, s22
	s_mov_b32 s27, s23
	s_add_i32 s34, s33, 0xc000
	s_mov_b32 m0, s34
	s_nop 0
	buffer_load_dwordx4 v174, s[24:27], s36 offen lds
	s_add_i32 s10, s33, 0x4000
	s_movk_i32 s37, 0x1000
	s_mov_b32 m0, s10
	s_nop 0
	buffer_load_dwordx4 v174, s[20:23], s37 offen lds
	s_add_i32 s10, s33, 0x8000
	s_movk_i32 s11, 0x2000
	s_mov_b32 m0, s10
	s_nop 0
	buffer_load_dwordx4 v174, s[20:23], s11 offen lds
	s_lshl_b32 s10, s2, 7
	s_and_b32 s10, s10, 0x380
	s_lshl_b32 s11, s31, 2
	s_add_i32 s10, s10, s11
	s_or_b32 s10, s30, s10
	v_and_b32_e32 v172, 31, v0
	v_lshl_or_b32 v140, s10, 7, v1
	v_mov_b32_e32 v141, 0
	v_lshl_add_u64 v[6:7], v[140:141], 4, s[14:15]
	v_ashrrev_i32_e32 v9, 31, v140
	v_mov_b32_e32 v8, v140
	v_lshl_or_b32 v140, s10, 5, v172
	v_lshlrev_b64 v[4:5], 2, v[140:141]
	v_lshl_add_u64 v[2:3], s[16:17], 0, v[4:5]
	global_load_dword v2, v[2:3], off
	v_lshl_add_u64 v[8:9], v[8:9], 4, s[14:15]
	global_load_dwordx4 v[116:119], v[6:7], off
	global_load_dwordx4 v[120:123], v[8:9], off offset:1024
	s_load_dwordx4 s[12:15], s[0:1], 0x40
	s_load_dwordx2 s[10:11], s[0:1], 0x50
	v_lshlrev_b32_e32 v173, 2, v1
	v_lshl_or_b32 v3, s28, 11, v173
	s_waitcnt lgkmcnt(0)
	global_load_dword v44, v3, s[14:15] offset:256
	global_load_dword v45, v3, s[14:15]
	v_bfe_u32 v175, v0, 5, 1
	v_lshlrev_b32_e32 v0, 11, v175
	v_lshlrev_b32_e32 v3, 4, v172
	s_add_i32 s0, s38, 0
	v_lshl_add_u64 v[4:5], s[12:13], 0, v[4:5]
	v_add3_u32 v176, s0, v0, v3
	global_load_dword v0, v[4:5], off
	v_lshrrev_b32_e32 v124, 2, v1
	v_lshrrev_b32_e32 v125, 4, v1
	v_xor_b32_e32 v124, v124, v125
	v_and_b32_e32 v124, 1, v124
	v_add_u32_e32 v124, -1, v124
	v_and_b32_e32 v124, 0x38383838, v124
	v_mov_b32_e32 v200, 0
	v_mov_b32_e32 v201, 0
	v_mov_b32_e32 v202, 0
	v_mov_b32_e32 v203, 0
	v_mov_b32_e32 v204, 0
	v_mov_b32_e32 v125, v124
	v_mov_b32_e32 v126, v124
	v_mov_b32_e32 v127, v124
	v_mov_b32_e32 v128, v124
	v_mov_b32_e32 v129, v124
	v_mov_b32_e32 v130, v124
	v_mov_b32_e32 v131, v124
	v_mov_b32_e32 v140, 0x7f7f7f7f
	s_mov_b32 s0, 0xf800000
	s_movk_i32 s15, 0x3000
	s_mov_b32 s12, -1
	s_movk_i32 s14, 0x4000
	s_mov_b32 s13, 0x8000
	v_mov_b32_e32 v132, v141
	v_mov_b32_e32 v133, v141
	v_mov_b32_e32 v134, v141
	v_mov_b32_e32 v135, v141
	v_mov_b32_e32 v136, v141
	v_mov_b32_e32 v137, v141
	v_mov_b32_e32 v138, v141
	v_mov_b32_e32 v139, v141
	v_mov_b32_e32 v52, v141
	v_mov_b32_e32 v53, v141
	v_mov_b32_e32 v54, v141
	v_mov_b32_e32 v55, v141
	v_mov_b32_e32 v56, v141
	v_mov_b32_e32 v57, v141
	v_mov_b32_e32 v58, v141
	v_mov_b32_e32 v59, v141
	v_mov_b32_e32 v60, v141
	v_mov_b32_e32 v61, v141
	v_mov_b32_e32 v62, v141
	v_mov_b32_e32 v63, v141
	v_mov_b32_e32 v64, v141
	v_mov_b32_e32 v65, v141
	v_mov_b32_e32 v66, v141
	v_mov_b32_e32 v67, v141
	s_waitcnt vmcnt(5)
	v_mov_b32_e32 v4, v2
	v_mov_b32_e32 v5, v2
	v_mov_b32_e32 v6, v2
	v_mov_b32_e32 v7, v2
	v_mov_b32_e32 v8, v2
	v_mov_b32_e32 v9, v2
	v_mov_b32_e32 v10, v2
	v_mov_b32_e32 v11, v2
	v_mov_b32_e32 v12, v2
	v_mov_b32_e32 v13, v2
	v_mov_b32_e32 v14, v2
	v_mov_b32_e32 v15, v2
	v_mov_b32_e32 v16, v2
	v_mov_b32_e32 v17, v2
	v_mov_b32_e32 v3, v2
	v_mov_b64_e32 v[18:19], v[16:17]
	v_mov_b64_e32 v[16:17], v[14:15]
	v_mov_b64_e32 v[14:15], v[12:13]
	v_mov_b64_e32 v[12:13], v[10:11]
	v_mov_b64_e32 v[10:11], v[8:9]
	v_mov_b64_e32 v[8:9], v[6:7]
	v_mov_b64_e32 v[6:7], v[4:5]
	v_mov_b64_e32 v[4:5], v[2:3]
	s_waitcnt vmcnt(0) lgkmcnt(0)
	s_barrier
	ds_read_b128 v[24:27], v176 offset:1024
	ds_read_b128 v[20:23], v176
	ds_read_b128 v[36:39], v176 offset:512
	ds_read_b128 v[40:43], v176 offset:1536
	ds_read_b128 v[84:87], v176 offset:16384
	ds_read_b128 v[92:95], v176 offset:16896
	ds_read_b128 v[88:91], v176 offset:17408
	ds_read_b128 v[96:99], v176 offset:17920
	s_waitcnt vmcnt(3) lgkmcnt(6)
	v_mfma_f32_32x32x64_f8f6f4 v[20:35], v[20:27], v[116:123], v[4:19]
	v_mbcnt_lo_u32_b32 v3, -1, 0
	v_mbcnt_hi_u32_b32 v46, -1, v3
	v_and_b32_e32 v3, 64, v46
	v_xor_b32_e32 v47, 32, v46
	v_add_u32_e32 v48, 64, v3
	s_waitcnt vmcnt(2)
	v_max_f32_e32 v3, v44, v44
	s_waitcnt vmcnt(1)
	v_max_f32_e32 v44, v45, v45
	v_max_f32_e32 v44, v44, v3
	v_cmp_lt_i32_e32 vcc, v47, v48
	s_waitcnt vmcnt(0) lgkmcnt(0)
	s_barrier
	s_mov_b32 m0, s33
	s_nop 0
	buffer_load_dwordx4 v174, s[20:23], s15 offen lds
	s_add_i32 s15, s34, 0x4000
	s_mov_b32 m0, s15
	s_nop 0
	buffer_load_dwordx4 v174, s[24:27], s37 offen lds
	s_waitcnt lgkmcnt(4)
	v_mfma_f32_32x32x64_f8f6f4 v[4:19], v[36:43], v[116:123], v[4:19]
	s_nop 1
	v_max_f32_e32 v3, v21, v21
	v_max_f32_e32 v36, v20, v20
	v_max_f32_e32 v3, v36, v3
	v_xor_b32_e32 v38, 16, v46
	s_nop 13
	v_max3_f32 v37, v22, v23, v5
	v_max3_f32 v36, v37, v26, v27
	v_cndmask_b32_e32 v37, v46, v47, vcc
	v_lshlrev_b32_e32 v37, 2, v37
	ds_bpermute_b32 v37, v37, v44
	v_cmp_lt_i32_e32 vcc, v38, v48
	v_max3_f32 v3, v3, v4, v6
	v_max3_f32 v3, v3, v7, v24
	v_cndmask_b32_e32 v38, v46, v38, vcc
	s_waitcnt lgkmcnt(0)
	v_max_f32_e32 v37, v37, v37
	v_max_f32_e32 v37, v44, v37
	v_lshlrev_b32_e32 v38, 2, v38
	ds_bpermute_b32 v38, v38, v37
	v_max3_f32 v36, v36, v10, v11
	v_max3_f32 v3, v3, v25, v8
	v_max3_f32 v36, v36, v30, v31
	v_max3_f32 v3, v3, v9, v28
	s_waitcnt lgkmcnt(0)
	v_max_f32_e32 v38, v38, v38
	v_max_f32_e32 v37, v37, v38
	v_xor_b32_e32 v38, 8, v46
	v_cmp_lt_i32_e32 vcc, v38, v48
	v_max3_f32 v36, v36, v14, v15
	v_max3_f32 v3, v3, v29, v12
	v_cndmask_b32_e32 v38, v46, v38, vcc
	v_lshlrev_b32_e32 v38, 2, v38
	ds_bpermute_b32 v38, v38, v37
	v_max3_f32 v36, v36, v34, v35
	v_max3_f32 v3, v3, v13, v32
	v_max3_f32 v36, v36, v18, v19
	v_max3_f32 v3, v3, v33, v16
	s_waitcnt lgkmcnt(0)
	v_max_f32_e32 v38, v38, v38
	v_max_f32_e32 v37, v37, v38
	v_xor_b32_e32 v38, 4, v46
	v_cmp_lt_i32_e32 vcc, v38, v48
	v_max3_f32 v3, v3, v17, v36
	v_mov_b32_e32 v36, v3
	v_cndmask_b32_e32 v38, v46, v38, vcc
	v_lshlrev_b32_e32 v38, 2, v38
	ds_bpermute_b32 v38, v38, v37
	v_permlane32_swap_b32_e32 v3, v36
	v_max_f32_e32 v36, v36, v36
	v_max_f32_e32 v3, v3, v3
	s_waitcnt lgkmcnt(0)
	v_max_f32_e32 v38, v38, v38
	v_max_f32_e32 v37, v37, v38
	v_xor_b32_e32 v38, 2, v46
	v_cmp_lt_i32_e32 vcc, v38, v48
	v_max_f32_e32 v3, v3, v36
	v_sub_f32_e32 v36, 0xc0400000, v3
	v_cndmask_b32_e32 v38, v46, v38, vcc
	v_lshlrev_b32_e32 v38, 2, v38
	ds_bpermute_b32 v38, v38, v37
	v_add_f32_e32 v20, v36, v20
	v_add_f32_e32 v21, v36, v21
	v_add_f32_e32 v22, v36, v22
	v_add_f32_e32 v23, v36, v23
	s_waitcnt lgkmcnt(0)
	v_max_f32_e32 v38, v38, v38
	v_max_f32_e32 v37, v37, v38
	v_xor_b32_e32 v38, 1, v46
	v_cmp_lt_i32_e32 vcc, v38, v48
	v_add_f32_e32 v24, v36, v24
	v_add_f32_e32 v25, v36, v25
	v_cndmask_b32_e32 v38, v46, v38, vcc
	v_lshlrev_b32_e32 v38, 2, v38
	ds_bpermute_b32 v38, v38, v37
	v_add_f32_e32 v26, v36, v26
	v_add_f32_e32 v27, v36, v27
	v_add_f32_e32 v28, v36, v28
	v_add_f32_e32 v29, v36, v29
	s_waitcnt lgkmcnt(0)
	v_max_f32_e32 v38, v38, v38
	v_max_f32_e32 v37, v37, v38
	v_mul_f32_e32 v38, 0x4f800000, v37
	v_cmp_gt_f32_e32 vcc, s0, v37
	v_add_f32_e32 v30, v36, v30
	v_add_f32_e32 v31, v36, v31
	v_cndmask_b32_e32 v37, v37, v38, vcc
	v_sqrt_f32_e32 v38, v37
	v_add_f32_e32 v32, v36, v32
	v_add_f32_e32 v33, v36, v33
	v_add_f32_e32 v34, v36, v34
	v_add_f32_e32 v35, v36, v35
	v_add_f32_e32 v4, v36, v4
	v_add_f32_e32 v5, v36, v5
	v_add_f32_e32 v6, v36, v6
	v_add_f32_e32 v7, v36, v7
	v_add_f32_e32 v8, v36, v8
	v_add_f32_e32 v9, v36, v9
	v_add_f32_e32 v10, v36, v10
	v_add_f32_e32 v11, v36, v11
	v_add_f32_e32 v12, v36, v12
	v_add_f32_e32 v13, v36, v13
	v_add_f32_e32 v14, v36, v14
	v_add_f32_e32 v15, v36, v15
	v_add_f32_e32 v16, v36, v16
	v_add_f32_e32 v17, v36, v17
	v_add_f32_e32 v18, v36, v18
	v_add_f32_e32 v19, v36, v19
	v_add_u32_e32 v36, -1, v38
	v_fma_f32 v39, -v36, v38, v37
	v_cmp_ge_f32_e64 s[0:1], 0, v39
	v_add_u32_e32 v39, 1, v38
	v_exp_f32_e32 v161, v20
	v_cndmask_b32_e64 v36, v38, v36, s[0:1]
	v_fma_f32 v38, -v39, v38, v37
	v_cmp_lt_f32_e64 s[0:1], 0, v38
	v_exp_f32_e32 v100, v4
	v_exp_f32_e32 v163, v21
	v_cndmask_b32_e64 v36, v36, v39, s[0:1]
	v_mul_f32_e32 v38, 0x37800000, v36
	v_cndmask_b32_e32 v36, v36, v38, vcc
	v_mov_b32_e32 v38, 0x260
	v_cmp_class_f32_e32 vcc, v37, v38
	s_mov_b32 s0, 0x42700000
	v_exp_f32_e32 v148, v5
	v_cndmask_b32_e32 v36, v36, v37, vcc
	s_waitcnt vmcnt(0)
	v_mul_f32_e32 v0, v36, v0
	v_mul_f32_e32 v0, 0x3f91eb85, v0
	v_exp_f32_e32 v162, v22
	v_exp_f32_e32 v101, v6
	v_exp_f32_e32 v164, v23
	v_exp_f32_e32 v102, v7
	v_exp_f32_e32 v150, v24
	v_exp_f32_e32 v143, v8
	v_exp_f32_e32 v154, v25
	v_exp_f32_e32 v146, v9
	v_exp_f32_e32 v152, v26
	v_exp_f32_e32 v145, v10
	v_exp_f32_e32 v157, v27
	v_exp_f32_e32 v147, v11
	v_exp_f32_e32 v149, v28
	v_exp_f32_e32 v69, v12
	v_exp_f32_e32 v153, v29
	v_exp_f32_e32 v109, v13
	v_exp_f32_e32 v151, v30
	v_exp_f32_e32 v108, v14
	v_exp_f32_e32 v156, v31
	v_exp_f32_e32 v142, v15
	v_exp_f32_e32 v155, v32
	v_exp_f32_e32 v110, v16
	v_exp_f32_e32 v159, v33
	v_exp_f32_e32 v144, v17
	v_exp_f32_e32 v158, v34
	v_exp_f32_e32 v111, v18
	v_exp_f32_e32 v160, v35
	v_exp_f32_e32 v114, v19
	v_cmp_nge_f32_e64 s[0:1], s0, v0
	v_sub_f32_e32 v0, v2, v3
	v_add_f32_e32 v36, 0xc0400000, v0
	v_mov_b32_e32 v37, v36
	v_mov_b32_e32 v38, v36
	v_mov_b32_e32 v39, v36
	v_mov_b32_e32 v40, v36
	v_mov_b32_e32 v41, v36
	v_mov_b32_e32 v42, v36
	v_mov_b32_e32 v43, v36
	v_mov_b32_e32 v44, v36
	v_mov_b32_e32 v45, v36
	v_mov_b32_e32 v46, v36
	v_mov_b32_e32 v47, v36
	v_mov_b32_e32 v48, v36
	v_mov_b32_e32 v49, v36
	v_mov_b32_e32 v50, v36
	v_mov_b32_e32 v51, v36
	v_mov_b32_e32 v4, v141
	v_mov_b32_e32 v5, v141
	v_mov_b32_e32 v6, v141
	v_mov_b32_e32 v7, v141
	v_mov_b32_e32 v8, v141
	v_mov_b32_e32 v9, v141
	v_mov_b32_e32 v10, v141
	v_mov_b32_e32 v11, v141
	v_mov_b32_e32 v12, v141
	v_mov_b32_e32 v13, v141
	v_mov_b32_e32 v14, v141
	v_mov_b32_e32 v15, v141
	v_mov_b32_e32 v16, v141
	v_mov_b32_e32 v17, v141
	v_mov_b32_e32 v18, v141
	v_mov_b32_e32 v19, v141
	v_mov_b32_e32 v20, v141
	v_mov_b32_e32 v21, v141
	v_mov_b32_e32 v22, v141
	v_mov_b32_e32 v23, v141
	v_mov_b32_e32 v24, v141
	v_mov_b32_e32 v25, v141
	v_mov_b32_e32 v26, v141
	v_mov_b32_e32 v27, v141
	v_mov_b32_e32 v28, v141
	v_mov_b32_e32 v29, v141
	v_mov_b32_e32 v30, v141
	v_mov_b32_e32 v31, v141
	v_mov_b32_e32 v32, v141
	v_mov_b32_e32 v33, v141
	v_mov_b32_e32 v34, v141
	v_mov_b32_e32 v35, v141
	v_mov_b32_e32 v0, v141
